# speedup vs baseline: 1.0077x; 1.0057x over previous
.LBB0_21:
	v_exp_f32_e64 v156, -|v154|
	v_max_f32 v157, 0, v154
	v_add_f32 v156, 1.0, v156
	v_log_f32 v156, v156
	s_nop 0
	v_fma_mixlo_f16 v155, v156, 1.0, v157
	ds_write_b16 v148, v155
	s_nop 3
	ds_read_b128 v[154:157], v139
	s_waitcnt lgkmcnt(1)
	s_barrier
	ds_read_b128 v[158:161], v140
	s_waitcnt lgkmcnt(1)
	v_mfma_f32_16x16x32_f16 v[162:165], v[154:157], v[6:9], v[106:109]
	ds_read_b128 v[166:169], v141
	v_mfma_f32_16x16x32_f16 v[154:157], v[154:157], v[26:29], v[110:113]
	ds_read_b128 v[170:173], v142
	v_mul_f32 v182, -2.0, v153
	s_waitcnt lgkmcnt(2)
	v_mfma_f32_16x16x32_f16 v[162:165], v[158:161], v[10:13], v[162:165]
	v_mfma_f32_16x16x32_f16 v[154:157], v[158:161], v[30:33], v[154:157]
	s_waitcnt lgkmcnt(1)
	v_mfma_f32_16x16x32_f16 v[158:161], v[166:169], v[14:17], v[162:165]
	v_mfma_f32_16x16x32_f16 v[154:157], v[166:169], v[34:37], v[154:157]
	s_waitcnt lgkmcnt(0)
	v_mfma_f32_16x16x32_f16 v[158:161], v[170:173], v[18:21], v[158:161]
	v_mfma_f32_16x16x32_f16 v[154:157], v[170:173], v[38:41], v[154:157]
	s_nop 7
	v_cndmask_b32_e64 v154, v158, v154, s[0:1]
	v_exp_f32_e64 v156, -|v154|
	v_max_f32 v157, 0, v154
	v_add_f32 v156, 1.0, v156
	v_log_f32 v156, v156
	s_nop 0
	v_fma_mixlo_f16 v155, v156, 1.0, v157
	ds_write_b16 v149, v155
	s_nop 3
	ds_read_b128 v[154:157], v143
	s_waitcnt lgkmcnt(1)
	s_barrier
	ds_read_b128 v[158:161], v144
	s_waitcnt lgkmcnt(1)
	v_mfma_f32_16x16x32_f16 v[162:165], v[154:157], v[42:45], v[114:117]
	ds_read_b128 v[166:169], v145
	v_mfma_f32_16x16x32_f16 v[170:173], v[154:157], v[58:61], v[118:121]
	ds_read_b128 v[174:177], v146
	v_mfma_f32_16x16x32_f16 v[178:181], v[154:157], v[74:77], v[122:125]
	v_mfma_f32_16x16x32_f16 v[154:157], v[154:157], v[90:93], v[126:129]
	s_waitcnt lgkmcnt(2)
	v_mfma_f32_16x16x32_f16 v[162:165], v[158:161], v[46:49], v[162:165]
	v_mfma_f32_16x16x32_f16 v[170:173], v[158:161], v[62:65], v[170:173]
	v_mfma_f32_16x16x32_f16 v[178:181], v[158:161], v[78:81], v[178:181]
	v_mfma_f32_16x16x32_f16 v[154:157], v[158:161], v[94:97], v[154:157]
	s_waitcnt lgkmcnt(1)
	v_mfma_f32_16x16x32_f16 v[158:161], v[166:169], v[50:53], v[162:165]
	v_mfma_f32_16x16x32_f16 v[162:165], v[166:169], v[66:69], v[170:173]
	v_mfma_f32_16x16x32_f16 v[170:173], v[166:169], v[82:85], v[178:181]
	v_mfma_f32_16x16x32_f16 v[154:157], v[166:169], v[98:101], v[154:157]
	s_waitcnt lgkmcnt(0)
	v_mfma_f32_16x16x32_f16 v[158:161], v[174:177], v[54:57], v[158:161]
	v_mfma_f32_16x16x32_f16 v[162:165], v[174:177], v[70:73], v[162:165]
	v_mfma_f32_16x16x32_f16 v[166:169], v[174:177], v[86:89], v[170:173]
	v_mfma_f32_16x16x32_f16 v[154:157], v[174:177], v[102:105], v[154:157]
	s_nop 5
	v_cndmask_b32_e64 v170, v162, v158, s[6:7]
	v_cndmask_b32_e64 v170, v170, v166, s[0:1]
	v_cndmask_b32_e64 v170, v170, v154, s[4:5]
	v_exp_f32_e32 v170, v170
	s_nop 0
	v_add_f32_e32 v170, 1.0, v170
	v_rcp_f32_e32 v170, v170
	s_nop 0
	v_fmac_f32_e32 v153, v170, v182
	s_nop 1
	v_add_f32_dpp v153, v153, v153 quad_perm:[1,0,3,2] row_mask:0xf bank_mask:0xf bound_ctrl:1
	s_nop 1
	v_add_f32_dpp v153, v153, v153 quad_perm:[2,3,0,1] row_mask:0xf bank_mask:0xf bound_ctrl:1
	s_nop 1
	v_add_f32_dpp v153, v153, v153 row_half_mirror row_mask:0xf bank_mask:0xf bound_ctrl:1
	v_cvt_f16_f32_e32 v170, v153
	ds_write_b16 v150, v170
	s_waitcnt lgkmcnt(0)
	s_barrier
	ds_read_b128 v[154:157], v147
	s_waitcnt lgkmcnt(0)
	v_mfma_f32_16x16x32_f16 v[130:133], v[154:157], v[2:5], v[130:133]
	v_mfma_f32_16x16x32_f16 v[154:157], v[154:157], v[22:25], v[134:137]
	s_nop 2
	v_add_u32_e32 v134, s3, v151
	ds_read_b32 v135, v134
	s_nop 2
	v_cndmask_b32_e64 v136, v130, v154, s[0:1]
	v_exp_f32_e64 v158, -|v136|
	v_max_f32 v159, 0, v136
	v_add_f32 v158, 1.0, v158
	v_log_f32 v158, v158
	s_nop 0
	v_fma_mixlo_f16 v137, v158, 1.0, v159
	ds_write_b16 v148, v137
	s_nop 3
	ds_read_b128 v[158:161], v139
	s_waitcnt lgkmcnt(1)
	s_barrier
	ds_read_b128 v[162:165], v140
	v_add_f32_e32 v136, v152, v153
	s_waitcnt lgkmcnt(1)
	v_mfma_f32_16x16x32_f16 v[166:169], v[158:161], v[6:9], v[106:109]
	ds_read_b128 v[170:173], v141
	v_mfma_f32_16x16x32_f16 v[158:161], v[158:161], v[26:29], v[110:113]
	ds_read_b128 v[174:177], v142
	v_mul_f32 v137, -2.0, v135
	s_waitcnt lgkmcnt(2)
	v_mfma_f32_16x16x32_f16 v[166:169], v[162:165], v[10:13], v[166:169]
	v_mfma_f32_16x16x32_f16 v[158:161], v[162:165], v[30:33], v[158:161]
	s_waitcnt lgkmcnt(1)
	v_mfma_f32_16x16x32_f16 v[162:165], v[170:173], v[14:17], v[166:169]
	v_mfma_f32_16x16x32_f16 v[158:161], v[170:173], v[34:37], v[158:161]
	s_waitcnt lgkmcnt(0)
	v_mfma_f32_16x16x32_f16 v[162:165], v[174:177], v[18:21], v[162:165]
	v_mfma_f32_16x16x32_f16 v[158:161], v[174:177], v[38:41], v[158:161]
	s_nop 7
	v_cndmask_b32_e64 v152, v162, v158, s[0:1]
	v_exp_f32_e64 v158, -|v152|
	v_max_f32 v159, 0, v152
	v_add_f32 v158, 1.0, v158
	v_log_f32 v158, v158
	s_nop 0
	v_fma_mixlo_f16 v153, v158, 1.0, v159
	ds_write_b16 v149, v153
	s_nop 3
	ds_read_b128 v[158:161], v143
	s_waitcnt lgkmcnt(1)
	s_barrier
	ds_read_b128 v[162:165], v144
	s_waitcnt lgkmcnt(1)
	v_mfma_f32_16x16x32_f16 v[166:169], v[158:161], v[42:45], v[114:117]
	ds_read_b128 v[170:173], v145
	v_mfma_f32_16x16x32_f16 v[174:177], v[158:161], v[58:61], v[118:121]
	ds_read_b128 v[178:181], v146
	v_mfma_f32_16x16x32_f16 v[182:185], v[158:161], v[74:77], v[122:125]
	v_mfma_f32_16x16x32_f16 v[158:161], v[158:161], v[90:93], v[126:129]
	s_waitcnt lgkmcnt(2)
	v_mfma_f32_16x16x32_f16 v[166:169], v[162:165], v[46:49], v[166:169]
	v_mfma_f32_16x16x32_f16 v[174:177], v[162:165], v[62:65], v[174:177]
	v_mfma_f32_16x16x32_f16 v[182:185], v[162:165], v[78:81], v[182:185]
	v_mfma_f32_16x16x32_f16 v[158:161], v[162:165], v[94:97], v[158:161]
	s_waitcnt lgkmcnt(1)
	v_mfma_f32_16x16x32_f16 v[162:165], v[170:173], v[50:53], v[166:169]
	v_mfma_f32_16x16x32_f16 v[166:169], v[170:173], v[66:69], v[174:177]
	v_mfma_f32_16x16x32_f16 v[174:177], v[170:173], v[82:85], v[182:185]
	v_mfma_f32_16x16x32_f16 v[158:161], v[170:173], v[98:101], v[158:161]
	s_waitcnt lgkmcnt(0)
	v_mfma_f32_16x16x32_f16 v[162:165], v[178:181], v[54:57], v[162:165]
	v_mfma_f32_16x16x32_f16 v[166:169], v[178:181], v[70:73], v[166:169]
	v_mfma_f32_16x16x32_f16 v[170:173], v[178:181], v[86:89], v[174:177]
	v_mfma_f32_16x16x32_f16 v[158:161], v[178:181], v[102:105], v[158:161]
	s_nop 5
	v_cndmask_b32_e64 v152, v166, v162, s[6:7]
	v_cndmask_b32_e64 v152, v152, v170, s[0:1]
	v_cndmask_b32_e64 v152, v152, v158, s[4:5]
	v_exp_f32_e32 v152, v152
	s_nop 0
	v_add_f32_e32 v152, 1.0, v152
	v_rcp_f32_e32 v152, v152
	s_nop 0
	v_fmac_f32_e32 v135, v152, v137
	s_nop 1
	v_add_f32_dpp v135, v135, v135 quad_perm:[1,0,3,2] row_mask:0xf bank_mask:0xf bound_ctrl:1
	s_nop 1
	v_add_f32_dpp v135, v135, v135 quad_perm:[2,3,0,1] row_mask:0xf bank_mask:0xf bound_ctrl:1
	s_nop 1
	v_add_f32_dpp v135, v135, v135 row_half_mirror row_mask:0xf bank_mask:0xf bound_ctrl:1
	v_cvt_f16_f32_e32 v137, v135
	ds_write_b16 v150, v137
	s_waitcnt lgkmcnt(0)
	s_barrier
	ds_read_b128 v[158:161], v147
	ds_read_b32 v137, v134 offset:32
	v_add_f32_e32 v135, v136, v135
	s_waitcnt lgkmcnt(1)
	v_mfma_f32_16x16x32_f16 v[130:133], v[158:161], v[2:5], v[130:133]
	v_mfma_f32_16x16x32_f16 v[152:155], v[158:161], v[22:25], v[154:157]
	s_nop 7
	v_cndmask_b32_e64 v156, v130, v152, s[0:1]
	v_exp_f32_e64 v158, -|v156|
	v_max_f32 v159, 0, v156
	v_add_f32 v158, 1.0, v158
	v_log_f32 v158, v158
	s_nop 0
	v_fma_mixlo_f16 v157, v158, 1.0, v159
	ds_write_b16 v148, v157
	s_nop 3
	ds_read_b128 v[156:159], v139
	s_waitcnt lgkmcnt(1)
	s_barrier
	ds_read_b128 v[160:163], v140
	s_waitcnt lgkmcnt(1)
	v_mfma_f32_16x16x32_f16 v[164:167], v[156:159], v[6:9], v[106:109]
	ds_read_b128 v[168:171], v141
	v_mfma_f32_16x16x32_f16 v[156:159], v[156:159], v[26:29], v[110:113]
	ds_read_b128 v[172:175], v142
	v_mul_f32 v136, -2.0, v137
	s_waitcnt lgkmcnt(2)
	v_mfma_f32_16x16x32_f16 v[164:167], v[160:163], v[10:13], v[164:167]
	v_mfma_f32_16x16x32_f16 v[156:159], v[160:163], v[30:33], v[156:159]
	s_waitcnt lgkmcnt(1)
	v_mfma_f32_16x16x32_f16 v[160:163], v[168:171], v[14:17], v[164:167]
	v_mfma_f32_16x16x32_f16 v[156:159], v[168:171], v[34:37], v[156:159]
	s_waitcnt lgkmcnt(0)
	v_mfma_f32_16x16x32_f16 v[160:163], v[172:175], v[18:21], v[160:163]
	v_mfma_f32_16x16x32_f16 v[156:159], v[172:175], v[38:41], v[156:159]
	s_nop 7
	v_cndmask_b32_e64 v156, v160, v156, s[0:1]
	v_exp_f32_e64 v158, -|v156|
	v_max_f32 v159, 0, v156
	v_add_f32 v158, 1.0, v158
	v_log_f32 v158, v158
	s_nop 0
	v_fma_mixlo_f16 v157, v158, 1.0, v159
	ds_write_b16 v149, v157
	s_nop 3
	ds_read_b128 v[156:159], v143
	s_waitcnt lgkmcnt(1)
	s_barrier
	ds_read_b128 v[160:163], v144
	s_waitcnt lgkmcnt(1)
	v_mfma_f32_16x16x32_f16 v[164:167], v[156:159], v[42:45], v[114:117]
	ds_read_b128 v[168:171], v145
	v_mfma_f32_16x16x32_f16 v[172:175], v[156:159], v[58:61], v[118:121]
	ds_read_b128 v[176:179], v146
	v_mfma_f32_16x16x32_f16 v[180:183], v[156:159], v[74:77], v[122:125]
	v_mfma_f32_16x16x32_f16 v[156:159], v[156:159], v[90:93], v[126:129]
	s_waitcnt lgkmcnt(2)
	v_mfma_f32_16x16x32_f16 v[164:167], v[160:163], v[46:49], v[164:167]
	v_mfma_f32_16x16x32_f16 v[172:175], v[160:163], v[62:65], v[172:175]
	v_mfma_f32_16x16x32_f16 v[180:183], v[160:163], v[78:81], v[180:183]
	v_mfma_f32_16x16x32_f16 v[156:159], v[160:163], v[94:97], v[156:159]
	s_waitcnt lgkmcnt(1)
	v_mfma_f32_16x16x32_f16 v[160:163], v[168:171], v[50:53], v[164:167]
	v_mfma_f32_16x16x32_f16 v[164:167], v[168:171], v[66:69], v[172:175]
	v_mfma_f32_16x16x32_f16 v[172:175], v[168:171], v[82:85], v[180:183]
	v_mfma_f32_16x16x32_f16 v[156:159], v[168:171], v[98:101], v[156:159]
	s_waitcnt lgkmcnt(0)
	v_mfma_f32_16x16x32_f16 v[160:163], v[176:179], v[54:57], v[160:163]
	v_mfma_f32_16x16x32_f16 v[164:167], v[176:179], v[70:73], v[164:167]
	v_mfma_f32_16x16x32_f16 v[168:171], v[176:179], v[86:89], v[172:175]
	v_mfma_f32_16x16x32_f16 v[156:159], v[176:179], v[102:105], v[156:159]
	s_nop 5
	v_cndmask_b32_e64 v172, v164, v160, s[6:7]
	v_cndmask_b32_e64 v172, v172, v168, s[0:1]
	v_cndmask_b32_e64 v172, v172, v156, s[4:5]
	v_exp_f32_e32 v172, v172
	s_nop 0
	v_add_f32_e32 v172, 1.0, v172
	v_rcp_f32_e32 v172, v172
	s_nop 0
	v_fmac_f32_e32 v137, v172, v136
	s_nop 1
	v_add_f32_dpp v136, v137, v137 quad_perm:[1,0,3,2] row_mask:0xf bank_mask:0xf bound_ctrl:1
	s_nop 1
	v_add_f32_dpp v136, v136, v136 quad_perm:[2,3,0,1] row_mask:0xf bank_mask:0xf bound_ctrl:1
	s_nop 1
	v_add_f32_dpp v136, v136, v136 row_half_mirror row_mask:0xf bank_mask:0xf bound_ctrl:1
	v_cvt_f16_f32_e32 v137, v136
	ds_write_b16 v150, v137
	s_waitcnt lgkmcnt(0)
	s_barrier
	ds_read_b128 v[156:159], v147
	ds_read_b32 v137, v134 offset:64
	v_add_f32_e32 v135, v135, v136
	s_waitcnt lgkmcnt(1)
	v_mfma_f32_16x16x32_f16 v[130:133], v[156:159], v[2:5], v[130:133]
	v_mfma_f32_16x16x32_f16 v[152:155], v[156:159], v[22:25], v[152:155]
	s_nop 7
	v_cndmask_b32_e64 v156, v130, v152, s[0:1]
	v_exp_f32_e64 v158, -|v156|
	v_max_f32 v159, 0, v156
	v_add_f32 v158, 1.0, v158
	v_log_f32 v158, v158
	s_nop 0
	v_fma_mixlo_f16 v157, v158, 1.0, v159
	ds_write_b16 v148, v157
	s_nop 3
	ds_read_b128 v[156:159], v139
	s_waitcnt lgkmcnt(1)
	s_barrier
	ds_read_b128 v[160:163], v140
	s_waitcnt lgkmcnt(1)
	v_mfma_f32_16x16x32_f16 v[164:167], v[156:159], v[6:9], v[106:109]
	ds_read_b128 v[168:171], v141
	v_mfma_f32_16x16x32_f16 v[156:159], v[156:159], v[26:29], v[110:113]
	ds_read_b128 v[172:175], v142
	v_mul_f32 v136, -2.0, v137
	s_waitcnt lgkmcnt(2)
	v_mfma_f32_16x16x32_f16 v[164:167], v[160:163], v[10:13], v[164:167]
	v_mfma_f32_16x16x32_f16 v[156:159], v[160:163], v[30:33], v[156:159]
	s_waitcnt lgkmcnt(1)
	v_mfma_f32_16x16x32_f16 v[160:163], v[168:171], v[14:17], v[164:167]
	v_mfma_f32_16x16x32_f16 v[156:159], v[168:171], v[34:37], v[156:159]
	s_waitcnt lgkmcnt(0)
	v_mfma_f32_16x16x32_f16 v[160:163], v[172:175], v[18:21], v[160:163]
	v_mfma_f32_16x16x32_f16 v[156:159], v[172:175], v[38:41], v[156:159]
	s_nop 7
	v_cndmask_b32_e64 v156, v160, v156, s[0:1]
	v_exp_f32_e64 v158, -|v156|
	v_max_f32 v159, 0, v156
	v_add_f32 v158, 1.0, v158
	v_log_f32 v158, v158
	s_nop 0
	v_fma_mixlo_f16 v157, v158, 1.0, v159
	ds_write_b16 v149, v157
	s_nop 3
	ds_read_b128 v[156:159], v143
	s_waitcnt lgkmcnt(1)
	s_barrier
	ds_read_b128 v[160:163], v144
	s_waitcnt lgkmcnt(1)
	v_mfma_f32_16x16x32_f16 v[164:167], v[156:159], v[42:45], v[114:117]
	ds_read_b128 v[168:171], v145
	v_mfma_f32_16x16x32_f16 v[172:175], v[156:159], v[58:61], v[118:121]
	ds_read_b128 v[176:179], v146
	v_mfma_f32_16x16x32_f16 v[180:183], v[156:159], v[74:77], v[122:125]
	v_mfma_f32_16x16x32_f16 v[156:159], v[156:159], v[90:93], v[126:129]
	s_waitcnt lgkmcnt(2)
	v_mfma_f32_16x16x32_f16 v[164:167], v[160:163], v[46:49], v[164:167]
	v_mfma_f32_16x16x32_f16 v[172:175], v[160:163], v[62:65], v[172:175]
	v_mfma_f32_16x16x32_f16 v[180:183], v[160:163], v[78:81], v[180:183]
	v_mfma_f32_16x16x32_f16 v[156:159], v[160:163], v[94:97], v[156:159]
	s_waitcnt lgkmcnt(1)
	v_mfma_f32_16x16x32_f16 v[160:163], v[168:171], v[50:53], v[164:167]
	v_mfma_f32_16x16x32_f16 v[164:167], v[168:171], v[66:69], v[172:175]
	v_mfma_f32_16x16x32_f16 v[172:175], v[168:171], v[82:85], v[180:183]
	v_mfma_f32_16x16x32_f16 v[156:159], v[168:171], v[98:101], v[156:159]
	s_waitcnt lgkmcnt(0)
	v_mfma_f32_16x16x32_f16 v[160:163], v[176:179], v[54:57], v[160:163]
	v_mfma_f32_16x16x32_f16 v[164:167], v[176:179], v[70:73], v[164:167]
	v_mfma_f32_16x16x32_f16 v[168:171], v[176:179], v[86:89], v[172:175]
	v_mfma_f32_16x16x32_f16 v[156:159], v[176:179], v[102:105], v[156:159]
	s_nop 5
	v_cndmask_b32_e64 v172, v164, v160, s[6:7]
	v_cndmask_b32_e64 v172, v172, v168, s[0:1]
	v_cndmask_b32_e64 v172, v172, v156, s[4:5]
	v_exp_f32_e32 v172, v172
	s_nop 0
	v_add_f32_e32 v172, 1.0, v172
	v_rcp_f32_e32 v172, v172
	s_nop 0
	v_fmac_f32_e32 v137, v172, v136
	s_nop 1
	v_add_f32_dpp v136, v137, v137 quad_perm:[1,0,3,2] row_mask:0xf bank_mask:0xf bound_ctrl:1
	s_nop 1
	v_add_f32_dpp v136, v136, v136 quad_perm:[2,3,0,1] row_mask:0xf bank_mask:0xf bound_ctrl:1
	s_nop 1
	v_add_f32_dpp v136, v136, v136 row_half_mirror row_mask:0xf bank_mask:0xf bound_ctrl:1
	v_cvt_f16_f32_e32 v137, v136
	ds_write_b16 v150, v137
	s_waitcnt lgkmcnt(0)
	s_barrier
	ds_read_b128 v[156:159], v147
	ds_read_b32 v137, v134 offset:96
	v_add_f32_e32 v135, v135, v136
	s_waitcnt lgkmcnt(1)
	v_mfma_f32_16x16x32_f16 v[130:133], v[156:159], v[2:5], v[130:133]
	v_mfma_f32_16x16x32_f16 v[152:155], v[156:159], v[22:25], v[152:155]
	s_nop 7
	v_cndmask_b32_e64 v156, v130, v152, s[0:1]
	v_exp_f32_e64 v158, -|v156|
	v_max_f32 v159, 0, v156
	v_add_f32 v158, 1.0, v158
	v_log_f32 v158, v158
	s_nop 0
	v_fma_mixlo_f16 v157, v158, 1.0, v159
	ds_write_b16 v148, v157
	s_nop 3
	ds_read_b128 v[156:159], v139
	s_waitcnt lgkmcnt(1)
	s_barrier
	ds_read_b128 v[160:163], v140
	s_waitcnt lgkmcnt(1)
	v_mfma_f32_16x16x32_f16 v[164:167], v[156:159], v[6:9], v[106:109]
	ds_read_b128 v[168:171], v141
	v_mfma_f32_16x16x32_f16 v[156:159], v[156:159], v[26:29], v[110:113]
	ds_read_b128 v[172:175], v142
	v_mul_f32 v136, -2.0, v137
	s_waitcnt lgkmcnt(2)
	v_mfma_f32_16x16x32_f16 v[164:167], v[160:163], v[10:13], v[164:167]
	v_mfma_f32_16x16x32_f16 v[156:159], v[160:163], v[30:33], v[156:159]
	s_waitcnt lgkmcnt(1)
	v_mfma_f32_16x16x32_f16 v[160:163], v[168:171], v[14:17], v[164:167]
	v_mfma_f32_16x16x32_f16 v[156:159], v[168:171], v[34:37], v[156:159]
	s_waitcnt lgkmcnt(0)
	v_mfma_f32_16x16x32_f16 v[160:163], v[172:175], v[18:21], v[160:163]
	v_mfma_f32_16x16x32_f16 v[156:159], v[172:175], v[38:41], v[156:159]
	s_nop 7
	v_cndmask_b32_e64 v156, v160, v156, s[0:1]
	v_exp_f32_e64 v158, -|v156|
	v_max_f32 v159, 0, v156
	v_add_f32 v158, 1.0, v158
	v_log_f32 v158, v158
	s_nop 0
	v_fma_mixlo_f16 v157, v158, 1.0, v159
	ds_write_b16 v149, v157
	s_nop 3
	ds_read_b128 v[156:159], v143
	s_waitcnt lgkmcnt(1)
	s_barrier
	ds_read_b128 v[160:163], v144
	s_waitcnt lgkmcnt(1)
	v_mfma_f32_16x16x32_f16 v[164:167], v[156:159], v[42:45], v[114:117]
	ds_read_b128 v[168:171], v145
	v_mfma_f32_16x16x32_f16 v[172:175], v[156:159], v[58:61], v[118:121]
	ds_read_b128 v[176:179], v146
	v_mfma_f32_16x16x32_f16 v[180:183], v[156:159], v[74:77], v[122:125]
	v_mfma_f32_16x16x32_f16 v[156:159], v[156:159], v[90:93], v[126:129]
	s_waitcnt lgkmcnt(2)
	v_mfma_f32_16x16x32_f16 v[164:167], v[160:163], v[46:49], v[164:167]
	v_mfma_f32_16x16x32_f16 v[172:175], v[160:163], v[62:65], v[172:175]
	v_mfma_f32_16x16x32_f16 v[180:183], v[160:163], v[78:81], v[180:183]
	v_mfma_f32_16x16x32_f16 v[156:159], v[160:163], v[94:97], v[156:159]
	s_waitcnt lgkmcnt(1)
	v_mfma_f32_16x16x32_f16 v[160:163], v[168:171], v[50:53], v[164:167]
	v_mfma_f32_16x16x32_f16 v[164:167], v[168:171], v[66:69], v[172:175]
	v_mfma_f32_16x16x32_f16 v[172:175], v[168:171], v[82:85], v[180:183]
	v_mfma_f32_16x16x32_f16 v[156:159], v[168:171], v[98:101], v[156:159]
	s_waitcnt lgkmcnt(0)
	v_mfma_f32_16x16x32_f16 v[160:163], v[176:179], v[54:57], v[160:163]
	v_mfma_f32_16x16x32_f16 v[164:167], v[176:179], v[70:73], v[164:167]
	v_mfma_f32_16x16x32_f16 v[168:171], v[176:179], v[86:89], v[172:175]
	v_mfma_f32_16x16x32_f16 v[156:159], v[176:179], v[102:105], v[156:159]
	s_nop 5
	v_cndmask_b32_e64 v172, v164, v160, s[6:7]
	v_cndmask_b32_e64 v172, v172, v168, s[0:1]
	v_cndmask_b32_e64 v172, v172, v156, s[4:5]
	v_exp_f32_e32 v172, v172
	s_nop 0
	v_add_f32_e32 v172, 1.0, v172
	v_rcp_f32_e32 v172, v172
	s_nop 0
	v_fmac_f32_e32 v137, v172, v136
	s_nop 1
	v_add_f32_dpp v136, v137, v137 quad_perm:[1,0,3,2] row_mask:0xf bank_mask:0xf bound_ctrl:1
	s_nop 1
	v_add_f32_dpp v136, v136, v136 quad_perm:[2,3,0,1] row_mask:0xf bank_mask:0xf bound_ctrl:1
	s_nop 1
	v_add_f32_dpp v136, v136, v136 row_half_mirror row_mask:0xf bank_mask:0xf bound_ctrl:1
	v_cvt_f16_f32_e32 v137, v136
	ds_write_b16 v150, v137
	s_waitcnt lgkmcnt(0)
	s_barrier
	ds_read_b128 v[156:159], v147
	ds_read_b32 v137, v134 offset:128
	v_add_f32_e32 v135, v135, v136
	s_waitcnt lgkmcnt(1)
	v_mfma_f32_16x16x32_f16 v[130:133], v[156:159], v[2:5], v[130:133]
	v_mfma_f32_16x16x32_f16 v[152:155], v[156:159], v[22:25], v[152:155]
	s_nop 7
	v_cndmask_b32_e64 v156, v130, v152, s[0:1]
	v_exp_f32_e64 v158, -|v156|
	v_max_f32 v159, 0, v156
	v_add_f32 v158, 1.0, v158
	v_log_f32 v158, v158
	s_nop 0
	v_fma_mixlo_f16 v157, v158, 1.0, v159
	ds_write_b16 v148, v157
	s_nop 3
	ds_read_b128 v[156:159], v139
	s_waitcnt lgkmcnt(1)
	s_barrier
	ds_read_b128 v[160:163], v140
	s_waitcnt lgkmcnt(1)
	v_mfma_f32_16x16x32_f16 v[164:167], v[156:159], v[6:9], v[106:109]
	ds_read_b128 v[168:171], v141
	v_mfma_f32_16x16x32_f16 v[156:159], v[156:159], v[26:29], v[110:113]
	ds_read_b128 v[172:175], v142
	v_mul_f32 v136, -2.0, v137
	s_waitcnt lgkmcnt(2)
	v_mfma_f32_16x16x32_f16 v[164:167], v[160:163], v[10:13], v[164:167]
	v_mfma_f32_16x16x32_f16 v[156:159], v[160:163], v[30:33], v[156:159]
	s_waitcnt lgkmcnt(1)
	v_mfma_f32_16x16x32_f16 v[160:163], v[168:171], v[14:17], v[164:167]
	v_mfma_f32_16x16x32_f16 v[156:159], v[168:171], v[34:37], v[156:159]
	s_waitcnt lgkmcnt(0)
	v_mfma_f32_16x16x32_f16 v[160:163], v[172:175], v[18:21], v[160:163]
	v_mfma_f32_16x16x32_f16 v[156:159], v[172:175], v[38:41], v[156:159]
	s_nop 7
	v_cndmask_b32_e64 v156, v160, v156, s[0:1]
	v_exp_f32_e64 v158, -|v156|
	v_max_f32 v159, 0, v156
	v_add_f32 v158, 1.0, v158
	v_log_f32 v158, v158
	s_nop 0
	v_fma_mixlo_f16 v157, v158, 1.0, v159
	ds_write_b16 v149, v157
	s_nop 3
	ds_read_b128 v[156:159], v143
	s_waitcnt lgkmcnt(1)
	s_barrier
	ds_read_b128 v[160:163], v144
	s_waitcnt lgkmcnt(1)
	v_mfma_f32_16x16x32_f16 v[164:167], v[156:159], v[42:45], v[114:117]
	ds_read_b128 v[168:171], v145
	v_mfma_f32_16x16x32_f16 v[172:175], v[156:159], v[58:61], v[118:121]
	ds_read_b128 v[176:179], v146
	v_mfma_f32_16x16x32_f16 v[180:183], v[156:159], v[74:77], v[122:125]
	v_mfma_f32_16x16x32_f16 v[156:159], v[156:159], v[90:93], v[126:129]
	s_waitcnt lgkmcnt(2)
	v_mfma_f32_16x16x32_f16 v[164:167], v[160:163], v[46:49], v[164:167]
	v_mfma_f32_16x16x32_f16 v[172:175], v[160:163], v[62:65], v[172:175]
	v_mfma_f32_16x16x32_f16 v[180:183], v[160:163], v[78:81], v[180:183]
	v_mfma_f32_16x16x32_f16 v[156:159], v[160:163], v[94:97], v[156:159]
	s_waitcnt lgkmcnt(1)
	v_mfma_f32_16x16x32_f16 v[160:163], v[168:171], v[50:53], v[164:167]
	v_mfma_f32_16x16x32_f16 v[164:167], v[168:171], v[66:69], v[172:175]
	v_mfma_f32_16x16x32_f16 v[172:175], v[168:171], v[82:85], v[180:183]
	v_mfma_f32_16x16x32_f16 v[156:159], v[168:171], v[98:101], v[156:159]
	s_waitcnt lgkmcnt(0)
	v_mfma_f32_16x16x32_f16 v[160:163], v[176:179], v[54:57], v[160:163]
	v_mfma_f32_16x16x32_f16 v[164:167], v[176:179], v[70:73], v[164:167]
	v_mfma_f32_16x16x32_f16 v[168:171], v[176:179], v[86:89], v[172:175]
	v_mfma_f32_16x16x32_f16 v[156:159], v[176:179], v[102:105], v[156:159]
	s_nop 5
	v_cndmask_b32_e64 v172, v164, v160, s[6:7]
	v_cndmask_b32_e64 v172, v172, v168, s[0:1]
	v_cndmask_b32_e64 v172, v172, v156, s[4:5]
	v_exp_f32_e32 v172, v172
	s_nop 0
	v_add_f32_e32 v172, 1.0, v172
	v_rcp_f32_e32 v172, v172
	s_nop 0
	v_fmac_f32_e32 v137, v172, v136
	s_nop 1
	v_add_f32_dpp v136, v137, v137 quad_perm:[1,0,3,2] row_mask:0xf bank_mask:0xf bound_ctrl:1
	s_nop 1
	v_add_f32_dpp v136, v136, v136 quad_perm:[2,3,0,1] row_mask:0xf bank_mask:0xf bound_ctrl:1
	s_nop 1
	v_add_f32_dpp v136, v136, v136 row_half_mirror row_mask:0xf bank_mask:0xf bound_ctrl:1
	v_cvt_f16_f32_e32 v137, v136
	ds_write_b16 v150, v137
	s_waitcnt lgkmcnt(0)
	s_barrier
	ds_read_b128 v[156:159], v147
	ds_read_b32 v137, v134 offset:160
	v_add_f32_e32 v135, v135, v136
	s_waitcnt lgkmcnt(1)
	v_mfma_f32_16x16x32_f16 v[130:133], v[156:159], v[2:5], v[130:133]
	v_mfma_f32_16x16x32_f16 v[152:155], v[156:159], v[22:25], v[152:155]
	s_nop 7
	v_cndmask_b32_e64 v156, v130, v152, s[0:1]
	v_exp_f32_e64 v158, -|v156|
	v_max_f32 v159, 0, v156
	v_add_f32 v158, 1.0, v158
	v_log_f32 v158, v158
	s_nop 0
	v_fma_mixlo_f16 v157, v158, 1.0, v159
	ds_write_b16 v148, v157
	s_nop 3
	ds_read_b128 v[156:159], v139
	s_waitcnt lgkmcnt(1)
	s_barrier
	ds_read_b128 v[160:163], v140
	s_waitcnt lgkmcnt(1)
	v_mfma_f32_16x16x32_f16 v[164:167], v[156:159], v[6:9], v[106:109]
	ds_read_b128 v[168:171], v141
	v_mfma_f32_16x16x32_f16 v[156:159], v[156:159], v[26:29], v[110:113]
	ds_read_b128 v[172:175], v142
	v_mul_f32 v136, -2.0, v137
	s_waitcnt lgkmcnt(2)
	v_mfma_f32_16x16x32_f16 v[164:167], v[160:163], v[10:13], v[164:167]
	v_mfma_f32_16x16x32_f16 v[156:159], v[160:163], v[30:33], v[156:159]
	s_waitcnt lgkmcnt(1)
	v_mfma_f32_16x16x32_f16 v[160:163], v[168:171], v[14:17], v[164:167]
	v_mfma_f32_16x16x32_f16 v[156:159], v[168:171], v[34:37], v[156:159]
	s_waitcnt lgkmcnt(0)
	v_mfma_f32_16x16x32_f16 v[160:163], v[172:175], v[18:21], v[160:163]
	v_mfma_f32_16x16x32_f16 v[156:159], v[172:175], v[38:41], v[156:159]
	s_nop 7
	v_cndmask_b32_e64 v156, v160, v156, s[0:1]
	v_exp_f32_e64 v158, -|v156|
	v_max_f32 v159, 0, v156
	v_add_f32 v158, 1.0, v158
	v_log_f32 v158, v158
	s_nop 0
	v_fma_mixlo_f16 v157, v158, 1.0, v159
	ds_write_b16 v149, v157
	s_nop 3
	ds_read_b128 v[156:159], v143
	s_waitcnt lgkmcnt(1)
	s_barrier
	ds_read_b128 v[160:163], v144
	s_waitcnt lgkmcnt(1)
	v_mfma_f32_16x16x32_f16 v[164:167], v[156:159], v[42:45], v[114:117]
	ds_read_b128 v[168:171], v145
	v_mfma_f32_16x16x32_f16 v[172:175], v[156:159], v[58:61], v[118:121]
	ds_read_b128 v[176:179], v146
	v_mfma_f32_16x16x32_f16 v[180:183], v[156:159], v[74:77], v[122:125]
	v_mfma_f32_16x16x32_f16 v[156:159], v[156:159], v[90:93], v[126:129]
	s_waitcnt lgkmcnt(2)
	v_mfma_f32_16x16x32_f16 v[164:167], v[160:163], v[46:49], v[164:167]
	v_mfma_f32_16x16x32_f16 v[172:175], v[160:163], v[62:65], v[172:175]
	v_mfma_f32_16x16x32_f16 v[180:183], v[160:163], v[78:81], v[180:183]
	v_mfma_f32_16x16x32_f16 v[156:159], v[160:163], v[94:97], v[156:159]
	s_waitcnt lgkmcnt(1)
	v_mfma_f32_16x16x32_f16 v[160:163], v[168:171], v[50:53], v[164:167]
	v_mfma_f32_16x16x32_f16 v[164:167], v[168:171], v[66:69], v[172:175]
	v_mfma_f32_16x16x32_f16 v[172:175], v[168:171], v[82:85], v[180:183]
	v_mfma_f32_16x16x32_f16 v[156:159], v[168:171], v[98:101], v[156:159]
	s_waitcnt lgkmcnt(0)
	v_mfma_f32_16x16x32_f16 v[160:163], v[176:179], v[54:57], v[160:163]
	v_mfma_f32_16x16x32_f16 v[164:167], v[176:179], v[70:73], v[164:167]
	v_mfma_f32_16x16x32_f16 v[168:171], v[176:179], v[86:89], v[172:175]
	v_mfma_f32_16x16x32_f16 v[156:159], v[176:179], v[102:105], v[156:159]
	s_nop 5
	v_cndmask_b32_e64 v172, v164, v160, s[6:7]
	v_cndmask_b32_e64 v172, v172, v168, s[0:1]
	v_cndmask_b32_e64 v172, v172, v156, s[4:5]
	v_exp_f32_e32 v172, v172
	s_nop 0
	v_add_f32_e32 v172, 1.0, v172
	v_rcp_f32_e32 v172, v172
	s_nop 0
	v_fmac_f32_e32 v137, v172, v136
	s_nop 1
	v_add_f32_dpp v136, v137, v137 quad_perm:[1,0,3,2] row_mask:0xf bank_mask:0xf bound_ctrl:1
	s_nop 1
	v_add_f32_dpp v136, v136, v136 quad_perm:[2,3,0,1] row_mask:0xf bank_mask:0xf bound_ctrl:1
	s_nop 1
	v_add_f32_dpp v136, v136, v136 row_half_mirror row_mask:0xf bank_mask:0xf bound_ctrl:1
	v_cvt_f16_f32_e32 v137, v136
	ds_write_b16 v150, v137
	s_waitcnt lgkmcnt(0)
	s_barrier
	ds_read_b128 v[156:159], v147
	ds_read_b32 v137, v134 offset:192
	v_add_f32_e32 v135, v135, v136
	s_waitcnt lgkmcnt(1)
	v_mfma_f32_16x16x32_f16 v[130:133], v[156:159], v[2:5], v[130:133]
	v_mfma_f32_16x16x32_f16 v[154:157], v[156:159], v[22:25], v[152:155]
	s_nop 7
	v_cndmask_b32_e64 v152, v130, v154, s[0:1]
	v_exp_f32_e64 v158, -|v152|
	v_max_f32 v159, 0, v152
	v_add_f32 v158, 1.0, v158
	v_log_f32 v158, v158
	s_nop 0
	v_fma_mixlo_f16 v153, v158, 1.0, v159
	ds_write_b16 v148, v153
	s_nop 3
	ds_read_b128 v[158:161], v139
	s_waitcnt lgkmcnt(1)
	s_barrier
	ds_read_b128 v[162:165], v140
	s_waitcnt lgkmcnt(1)
	v_mfma_f32_16x16x32_f16 v[166:169], v[158:161], v[6:9], v[106:109]
	ds_read_b128 v[170:173], v141
	v_mfma_f32_16x16x32_f16 v[158:161], v[158:161], v[26:29], v[110:113]
	ds_read_b128 v[174:177], v142
	v_mul_f32 v136, -2.0, v137
	s_waitcnt lgkmcnt(2)
	v_mfma_f32_16x16x32_f16 v[166:169], v[162:165], v[10:13], v[166:169]
	v_mfma_f32_16x16x32_f16 v[158:161], v[162:165], v[30:33], v[158:161]
	s_waitcnt lgkmcnt(1)
	v_mfma_f32_16x16x32_f16 v[162:165], v[170:173], v[14:17], v[166:169]
	v_mfma_f32_16x16x32_f16 v[158:161], v[170:173], v[34:37], v[158:161]
	s_waitcnt lgkmcnt(0)
	v_mfma_f32_16x16x32_f16 v[162:165], v[174:177], v[18:21], v[162:165]
	v_mfma_f32_16x16x32_f16 v[158:161], v[174:177], v[38:41], v[158:161]
	s_nop 7
	v_cndmask_b32_e64 v152, v162, v158, s[0:1]
	v_exp_f32_e64 v158, -|v152|
	v_max_f32 v159, 0, v152
	v_add_f32 v158, 1.0, v158
	v_log_f32 v158, v158
	s_nop 0
	v_fma_mixlo_f16 v153, v158, 1.0, v159
	ds_write_b16 v149, v153
	s_nop 3
	ds_read_b128 v[158:161], v143
	s_waitcnt lgkmcnt(1)
	s_barrier
	ds_read_b128 v[162:165], v144
	s_waitcnt lgkmcnt(1)
	v_mfma_f32_16x16x32_f16 v[166:169], v[158:161], v[42:45], v[114:117]
	ds_read_b128 v[170:173], v145
	v_mfma_f32_16x16x32_f16 v[174:177], v[158:161], v[58:61], v[118:121]
	ds_read_b128 v[178:181], v146
	v_mfma_f32_16x16x32_f16 v[182:185], v[158:161], v[74:77], v[122:125]
	v_mfma_f32_16x16x32_f16 v[158:161], v[158:161], v[90:93], v[126:129]
	s_waitcnt lgkmcnt(2)
	v_mfma_f32_16x16x32_f16 v[166:169], v[162:165], v[46:49], v[166:169]
	v_mfma_f32_16x16x32_f16 v[174:177], v[162:165], v[62:65], v[174:177]
	v_mfma_f32_16x16x32_f16 v[182:185], v[162:165], v[78:81], v[182:185]
	v_mfma_f32_16x16x32_f16 v[158:161], v[162:165], v[94:97], v[158:161]
	s_waitcnt lgkmcnt(1)
	v_mfma_f32_16x16x32_f16 v[162:165], v[170:173], v[50:53], v[166:169]
	v_mfma_f32_16x16x32_f16 v[166:169], v[170:173], v[66:69], v[174:177]
	v_mfma_f32_16x16x32_f16 v[174:177], v[170:173], v[82:85], v[182:185]
	v_mfma_f32_16x16x32_f16 v[158:161], v[170:173], v[98:101], v[158:161]
	s_waitcnt lgkmcnt(0)
	v_mfma_f32_16x16x32_f16 v[162:165], v[178:181], v[54:57], v[162:165]
	v_mfma_f32_16x16x32_f16 v[166:169], v[178:181], v[70:73], v[166:169]
	v_mfma_f32_16x16x32_f16 v[170:173], v[178:181], v[86:89], v[174:177]
	v_mfma_f32_16x16x32_f16 v[158:161], v[178:181], v[102:105], v[158:161]
	s_nop 5
	v_cndmask_b32_e64 v152, v166, v162, s[6:7]
	v_cndmask_b32_e64 v152, v152, v170, s[0:1]
	v_cndmask_b32_e64 v152, v152, v158, s[4:5]
	v_exp_f32_e32 v152, v152
	s_nop 0
	v_add_f32_e32 v152, 1.0, v152
	v_rcp_f32_e32 v152, v152
	s_nop 0
	v_fmac_f32_e32 v137, v152, v136
	s_nop 1
	v_add_f32_dpp v136, v137, v137 quad_perm:[1,0,3,2] row_mask:0xf bank_mask:0xf bound_ctrl:1
	s_nop 1
	v_add_f32_dpp v136, v136, v136 quad_perm:[2,3,0,1] row_mask:0xf bank_mask:0xf bound_ctrl:1
	s_nop 1
	v_add_f32_dpp v136, v136, v136 row_half_mirror row_mask:0xf bank_mask:0xf bound_ctrl:1
	v_cvt_f16_f32_e32 v137, v136
	ds_write_b16 v150, v137
	s_waitcnt lgkmcnt(0)
	s_barrier
	ds_read_b128 v[158:161], v147
	v_add_f32_e32 v152, v135, v136
	ds_read_b32 v153, v134 offset:224
	s_addk_i32 s3, 0x100
	s_cmpk_eq_u32 s3, 0xfa20
	s_waitcnt lgkmcnt(1)
	v_mfma_f32_16x16x32_f16 v[130:133], v[158:161], v[2:5], v[130:133]
	v_mfma_f32_16x16x32_f16 v[134:137], v[158:161], v[22:25], v[154:157]
	s_nop 7
	v_cndmask_b32_e64 v154, v130, v134, s[0:1]
	s_cbranch_scc0 .LBB0_21
	s_and_saveexec_b64 s[0:1], vcc
	ds_write_b32 v1, v152
	s_or_b64 exec, exec, s[0:1]
	v_cmp_gt_u32_e32 vcc, 10, v0
	s_waitcnt lgkmcnt(0)
	s_barrier
	s_and_saveexec_b64 s[0:1], vcc
	s_cbranch_execz .LBB0_28
	v_lshlrev_b32_e32 v1, 2, v0
	global_load_dword v1, v1, s[12:13]
	v_mov_b32_e32 v139, 0
	v_lshl_add_u64 v[2:3], s[10:11], 0, v[138:139]
	v_lshl_add_u64 v[2:3], v[2:3], 0, 28
	s_mov_b32 s0, 0
